# rolling gather (8-deep window, exact masks, L+bias folded) + write-through sc1 stores for T/L in GEMM and out in gather
# speedup vs baseline: 1.0229x; 1.0229x over previous
.LBB1_2:
	s_waitcnt vmcnt(0)
	v_cvt_pk_f16_f32 v3, v128, v129
	v_cvt_pk_f16_f32 v2, v126, v127
	ds_write_b64 v154, v[2:3]
	v_cvt_pk_f16_f32 v3, v104, v105
	v_cvt_pk_f16_f32 v2, v102, v103
	ds_write_b64 v154, v[2:3] offset:2176
	v_cvt_pk_f16_f32 v3, v100, v101
	v_cvt_pk_f16_f32 v2, v98, v99
	ds_write_b64 v154, v[2:3] offset:4352
	v_cvt_pk_f16_f32 v3, v112, v113
	v_cvt_pk_f16_f32 v2, v110, v111
	ds_write_b64 v154, v[2:3] offset:6528
	v_cvt_pk_f16_f32 v3, v108, v109
	v_cvt_pk_f16_f32 v2, v106, v107
	ds_write_b64 v154, v[2:3] offset:8704
	v_cvt_pk_f16_f32 v3, v120, v121
	v_cvt_pk_f16_f32 v2, v118, v119
	ds_write_b64 v154, v[2:3] offset:10880
	v_cvt_pk_f16_f32 v3, v116, v117
	v_cvt_pk_f16_f32 v2, v114, v115
	s_mov_b32 s14, s6
	ds_write_b64 v154, v[2:3] offset:13056
	v_cvt_pk_f16_f32 v3, v124, v125
	v_cvt_pk_f16_f32 v2, v122, v123
	s_cmp_lt_i32 s15, 0
	ds_write_b64 v154, v[2:3] offset:15232
	s_waitcnt lgkmcnt(0)
	s_barrier
	s_cbranch_scc1 .LBB1_36
	v_add_u32_e32 v8, v137, v153
	v_add_u32_e32 v2, 0x4000, v8
	ds_read2_b64 v[2:5], v2 offset0:128 offset1:136
	s_lshl_b32 s6, s15, 6
	s_and_saveexec_b64 s[10:11], s[4:5]
	s_xor_b64 s[10:11], exec, s[10:11]
	s_cbranch_execz .LBB1_5
	v_or_b32_e32 v6, s6, v145
	v_lshlrev_b32_e32 v132, 8, v6
	v_lshl_add_u64 v[6:7], v[130:131], 0, v[132:133]
	s_waitcnt lgkmcnt(0)
	global_store_dwordx4 v[6:7], v[2:5], off offset:-256 sc1
.LBB1_5:
	s_or_saveexec_b64 s[10:11], s[10:11]
	s_mul_i32 s16, s15, 0xa36f
	s_lshr_b32 s16, s16, 16
	s_sub_i32 s15, s15, s16
	s_bfe_u32 s15, s15, 0xf0001
	s_add_i32 s15, s15, s16
	s_mul_hi_u32 s16, s6, 0x68db8bad
	s_lshr_b32 s16, s16, 14
	s_mul_i32 s16, s16, 0x9c40
	s_lshr_b32 s15, s15, 8
	s_sub_i32 s16, s6, s16
	s_and_b32 s15, s15, 0xfe
	v_add_u32_e32 v6, s15, v152
	v_mov_b32_e32 v7, s16
	v_mad_u32_u24 v6, v6, s3, v7
	v_lshlrev_b32_e32 v7, 1, v151
	s_xor_b64 exec, exec, s[10:11]
	s_cbranch_execz .LBB1_7
	v_or_b32_e32 v9, v6, v145
	v_lshl_or_b32 v9, v9, 7, v7
	s_waitcnt lgkmcnt(0)
	global_store_dwordx4 v9, v[2:5], s[12:13] sc1
.LBB1_7:
	s_or_b64 exec, exec, s[10:11]
	s_waitcnt lgkmcnt(0)
	v_add_u32_e32 v2, v137, v150
	v_add_u32_e32 v2, 0x4000, v2
	ds_read2_b64 v[2:5], v2 offset0:128 offset1:136
	s_and_saveexec_b64 s[10:11], s[4:5]
	s_xor_b64 s[10:11], exec, s[10:11]
	s_cbranch_execz .LBB1_9
	v_or_b32_e32 v9, s6, v149
	v_lshlrev_b32_e32 v132, 8, v9
	v_lshl_add_u64 v[10:11], v[130:131], 0, v[132:133]
	s_waitcnt lgkmcnt(0)
	global_store_dwordx4 v[10:11], v[2:5], off offset:-256 sc1
.LBB1_9:
	s_andn2_saveexec_b64 s[10:11], s[10:11]
	s_cbranch_execz .LBB1_11
	v_or_b32_e32 v9, v6, v149
	v_lshl_or_b32 v9, v9, 7, v7
	s_waitcnt lgkmcnt(0)
	global_store_dwordx4 v9, v[2:5], s[12:13] sc1
.LBB1_11:
	s_or_b64 exec, exec, s[10:11]
	s_waitcnt lgkmcnt(0)
	v_add_u32_e32 v2, v137, v148
	v_add_u32_e32 v2, 0x4000, v2
	ds_read2_b64 v[2:5], v2 offset0:128 offset1:136
	s_and_saveexec_b64 s[10:11], s[4:5]
	s_xor_b64 s[10:11], exec, s[10:11]
	s_cbranch_execz .LBB1_13
	v_or_b32_e32 v9, s6, v147
	v_lshlrev_b32_e32 v132, 8, v9
	v_lshl_add_u64 v[10:11], v[130:131], 0, v[132:133]
	s_waitcnt lgkmcnt(0)
	global_store_dwordx4 v[10:11], v[2:5], off offset:-256 sc1
.LBB1_13:
	s_andn2_saveexec_b64 s[10:11], s[10:11]
	s_cbranch_execz .LBB1_15
	v_or_b32_e32 v9, v6, v147
	v_lshl_or_b32 v9, v9, 7, v7
	s_waitcnt lgkmcnt(0)
	global_store_dwordx4 v9, v[2:5], s[12:13] sc1
.LBB1_15:
	s_or_b64 exec, exec, s[10:11]
	s_waitcnt lgkmcnt(0)
	v_add_u32_e32 v2, v137, v146
	v_add_u32_e32 v2, 0x4000, v2
	ds_read2_b64 v[2:5], v2 offset0:128 offset1:136
	s_and_saveexec_b64 s[10:11], s[4:5]
	s_xor_b64 s[10:11], exec, s[10:11]
	s_cbranch_execz .LBB1_17
	v_or_b32_e32 v9, s6, v144
	v_lshlrev_b32_e32 v132, 8, v9
	v_lshl_add_u64 v[10:11], v[130:131], 0, v[132:133]
	s_waitcnt lgkmcnt(0)
	global_store_dwordx4 v[10:11], v[2:5], off offset:-256 sc1
.LBB1_17:
	s_andn2_saveexec_b64 s[10:11], s[10:11]
	s_cbranch_execz .LBB1_19
	v_or_b32_e32 v9, v6, v144
	v_lshl_or_b32 v9, v9, 7, v7
	s_waitcnt lgkmcnt(0)
	global_store_dwordx4 v9, v[2:5], s[12:13] sc1
.LBB1_19:
	s_or_b64 exec, exec, s[10:11]
	s_waitcnt lgkmcnt(0)
	v_add_u32_e32 v2, 0x8000, v8
	ds_read2_b64 v[2:5], v2 offset0:192 offset1:200
	s_and_saveexec_b64 s[10:11], s[4:5]
	s_xor_b64 s[10:11], exec, s[10:11]
	s_cbranch_execz .LBB1_21
	v_or_b32_e32 v8, s6, v143
	v_lshlrev_b32_e32 v132, 8, v8
	v_lshl_add_u64 v[8:9], v[130:131], 0, v[132:133]
	s_waitcnt lgkmcnt(0)
	global_store_dwordx4 v[8:9], v[2:5], off offset:-256 sc1
.LBB1_21:
	s_andn2_saveexec_b64 s[10:11], s[10:11]
	s_cbranch_execz .LBB1_23
	v_or_b32_e32 v8, v6, v143
	v_lshl_or_b32 v8, v8, 7, v7
	s_waitcnt lgkmcnt(0)
	global_store_dwordx4 v8, v[2:5], s[12:13] sc1
.LBB1_23:
	s_or_b64 exec, exec, s[10:11]
	s_waitcnt lgkmcnt(0)
	v_add_u32_e32 v2, v137, v142
	v_add_u32_e32 v2, 0x4000, v2
	ds_read2_b64 v[2:5], v2 offset0:128 offset1:136
	s_and_saveexec_b64 s[10:11], s[4:5]
	s_xor_b64 s[10:11], exec, s[10:11]
	s_cbranch_execz .LBB1_25
	v_add_lshl_u32 v132, s6, v141, 8
	v_lshl_add_u64 v[8:9], v[130:131], 0, v[132:133]
	s_waitcnt lgkmcnt(0)
	global_store_dwordx4 v[8:9], v[2:5], off offset:-256 sc1
.LBB1_25:
	s_andn2_saveexec_b64 s[10:11], s[10:11]
	s_cbranch_execz .LBB1_27
	v_add_u32_e32 v8, v6, v141
	v_lshl_or_b32 v8, v8, 7, v7
	s_waitcnt lgkmcnt(0)
	global_store_dwordx4 v8, v[2:5], s[12:13] sc1
.LBB1_27:
	s_or_b64 exec, exec, s[10:11]
	s_waitcnt lgkmcnt(0)
	v_add_u32_e32 v2, v137, v140
	v_add_u32_e32 v2, 0x4000, v2
	ds_read2_b64 v[2:5], v2 offset0:128 offset1:136
	s_and_saveexec_b64 s[10:11], s[4:5]
	s_xor_b64 s[10:11], exec, s[10:11]
	s_cbranch_execz .LBB1_29
	v_add_lshl_u32 v132, s6, v139, 8
	v_lshl_add_u64 v[8:9], v[130:131], 0, v[132:133]
	s_waitcnt lgkmcnt(0)
	global_store_dwordx4 v[8:9], v[2:5], off offset:-256 sc1
.LBB1_29:
	s_andn2_saveexec_b64 s[10:11], s[10:11]
	s_cbranch_execz .LBB1_31
	v_add_u32_e32 v8, v6, v139
	v_lshl_or_b32 v8, v8, 7, v7
	s_waitcnt lgkmcnt(0)
	global_store_dwordx4 v8, v[2:5], s[12:13] sc1
.LBB1_31:
	s_or_b64 exec, exec, s[10:11]
	s_waitcnt lgkmcnt(0)
	v_add_u32_e32 v2, v137, v138
	v_add_u32_e32 v2, 0x4000, v2
	ds_read2_b64 v[2:5], v2 offset0:128 offset1:136
	s_and_saveexec_b64 s[10:11], s[4:5]
	s_xor_b64 s[10:11], exec, s[10:11]
	s_cbranch_execz .LBB1_33
	v_add_lshl_u32 v132, s6, v136, 8
	v_lshl_add_u64 v[6:7], v[130:131], 0, v[132:133]
	s_waitcnt lgkmcnt(0)
	global_store_dwordx4 v[6:7], v[2:5], off offset:-256 sc1
.LBB1_33:
	s_andn2_saveexec_b64 s[10:11], s[10:11]
	s_cbranch_execz .LBB1_35
	v_add_u32_e32 v6, v6, v136
	v_lshl_or_b32 v6, v6, 7, v7
	s_waitcnt lgkmcnt(0)
	global_store_dwordx4 v6, v[2:5], s[12:13] sc1

.LBB1_40:
	s_mul_i32 s6, s14, 0xa36f
	s_lshr_b32 s6, s6, 16
	s_sub_i32 s7, s14, s6
	v_add_u32_e32 v8, v137, v153
	s_lshl_b32 s3, s14, 6
	s_bfe_u32 s7, s7, 0xf0001
	v_add_u32_e32 v2, 0x4000, v8
	s_add_i32 s7, s7, s6
	s_mul_hi_u32 s6, s3, 0x68db8bad
	ds_read2_b64 v[2:5], v2 offset0:128 offset1:136
	s_lshr_b32 s6, s6, 14
	s_mul_i32 s6, s6, 0x9c40
	s_lshr_b32 s7, s7, 8
	s_sub_i32 s6, s3, s6
	s_and_b32 s7, s7, 0xfe
	s_mov_b32 s8, 0x9c40
	v_add_u32_e32 v6, s7, v152
	v_mov_b32_e32 v7, s6
	s_and_saveexec_b64 s[6:7], s[4:5]
	s_xor_b64 s[6:7], exec, s[6:7]
	s_cbranch_execz .LBB1_42
	v_or_b32_e32 v9, s3, v145
	v_lshlrev_b32_e32 v10, 8, v9
	v_mov_b32_e32 v11, 0
	v_lshl_add_u64 v[10:11], v[130:131], 0, v[10:11]
	s_waitcnt lgkmcnt(0)
	global_store_dwordx4 v[10:11], v[2:5], off offset:-256 sc1
.LBB1_42:
	s_or_saveexec_b64 s[6:7], s[6:7]
	v_mad_u32_u24 v6, v6, s8, v7
	v_lshlrev_b32_e32 v7, 1, v151
	s_xor_b64 exec, exec, s[6:7]
	s_cbranch_execz .LBB1_44
	v_or_b32_e32 v9, v6, v145
	v_lshl_or_b32 v9, v9, 7, v7
	s_waitcnt lgkmcnt(0)
	global_store_dwordx4 v9, v[2:5], s[12:13] sc1
.LBB1_44:
	s_or_b64 exec, exec, s[6:7]
	s_waitcnt lgkmcnt(0)
	v_add_u32_e32 v2, v137, v150
	v_add_u32_e32 v2, 0x4000, v2
	ds_read2_b64 v[2:5], v2 offset0:128 offset1:136
	s_and_saveexec_b64 s[6:7], s[4:5]
	s_xor_b64 s[6:7], exec, s[6:7]
	s_cbranch_execz .LBB1_46
	v_or_b32_e32 v9, s3, v149
	v_lshlrev_b32_e32 v10, 8, v9
	v_mov_b32_e32 v11, 0
	v_lshl_add_u64 v[10:11], v[130:131], 0, v[10:11]
	s_waitcnt lgkmcnt(0)
	global_store_dwordx4 v[10:11], v[2:5], off offset:-256 sc1
.LBB1_46:
	s_andn2_saveexec_b64 s[6:7], s[6:7]
	s_cbranch_execz .LBB1_48
	v_or_b32_e32 v9, v6, v149
	v_lshl_or_b32 v9, v9, 7, v7
	s_waitcnt lgkmcnt(0)
	global_store_dwordx4 v9, v[2:5], s[12:13] sc1
.LBB1_48:
	s_or_b64 exec, exec, s[6:7]
	s_waitcnt lgkmcnt(0)
	v_add_u32_e32 v2, v137, v148
	v_add_u32_e32 v2, 0x4000, v2
	ds_read2_b64 v[2:5], v2 offset0:128 offset1:136
	s_and_saveexec_b64 s[6:7], s[4:5]
	s_xor_b64 s[6:7], exec, s[6:7]
	s_cbranch_execz .LBB1_50
	v_or_b32_e32 v9, s3, v147
	v_lshlrev_b32_e32 v10, 8, v9
	v_mov_b32_e32 v11, 0
	v_lshl_add_u64 v[10:11], v[130:131], 0, v[10:11]
	s_waitcnt lgkmcnt(0)
	global_store_dwordx4 v[10:11], v[2:5], off offset:-256 sc1
.LBB1_50:
	s_andn2_saveexec_b64 s[6:7], s[6:7]
	s_cbranch_execz .LBB1_52
	v_or_b32_e32 v9, v6, v147
	v_lshl_or_b32 v9, v9, 7, v7
	s_waitcnt lgkmcnt(0)
	global_store_dwordx4 v9, v[2:5], s[12:13] sc1
.LBB1_52:
	s_or_b64 exec, exec, s[6:7]
	s_waitcnt lgkmcnt(0)
	v_add_u32_e32 v2, v137, v146
	v_add_u32_e32 v2, 0x4000, v2
	ds_read2_b64 v[2:5], v2 offset0:128 offset1:136
	s_and_saveexec_b64 s[6:7], s[4:5]
	s_xor_b64 s[6:7], exec, s[6:7]
	s_cbranch_execz .LBB1_54
	v_or_b32_e32 v9, s3, v144
	v_lshlrev_b32_e32 v10, 8, v9
	v_mov_b32_e32 v11, 0
	v_lshl_add_u64 v[10:11], v[130:131], 0, v[10:11]
	s_waitcnt lgkmcnt(0)
	global_store_dwordx4 v[10:11], v[2:5], off offset:-256 sc1
.LBB1_54:
	s_andn2_saveexec_b64 s[6:7], s[6:7]
	s_cbranch_execz .LBB1_56
	v_or_b32_e32 v9, v6, v144
	v_lshl_or_b32 v9, v9, 7, v7
	s_waitcnt lgkmcnt(0)
	global_store_dwordx4 v9, v[2:5], s[12:13] sc1
.LBB1_56:
	s_or_b64 exec, exec, s[6:7]
	s_waitcnt lgkmcnt(0)
	v_add_u32_e32 v2, 0x8000, v8
	ds_read2_b64 v[2:5], v2 offset0:192 offset1:200
	s_and_saveexec_b64 s[6:7], s[4:5]
	s_xor_b64 s[6:7], exec, s[6:7]
	s_cbranch_execz .LBB1_58
	v_or_b32_e32 v8, s3, v143
	v_lshlrev_b32_e32 v8, 8, v8
	v_mov_b32_e32 v9, 0
	v_lshl_add_u64 v[8:9], v[130:131], 0, v[8:9]
	s_waitcnt lgkmcnt(0)
	global_store_dwordx4 v[8:9], v[2:5], off offset:-256 sc1
.LBB1_58:
	s_andn2_saveexec_b64 s[6:7], s[6:7]
	s_cbranch_execz .LBB1_60
	v_or_b32_e32 v8, v6, v143
	v_lshl_or_b32 v8, v8, 7, v7
	s_waitcnt lgkmcnt(0)
	global_store_dwordx4 v8, v[2:5], s[12:13] sc1
.LBB1_60:
	s_or_b64 exec, exec, s[6:7]
	s_waitcnt lgkmcnt(0)
	v_add_u32_e32 v2, v137, v142
	v_add_u32_e32 v2, 0x4000, v2
	ds_read2_b64 v[2:5], v2 offset0:128 offset1:136
	s_and_saveexec_b64 s[6:7], s[4:5]
	s_xor_b64 s[6:7], exec, s[6:7]
	s_cbranch_execz .LBB1_62
	v_add_lshl_u32 v8, s3, v141, 8
	v_mov_b32_e32 v9, 0
	v_lshl_add_u64 v[8:9], v[130:131], 0, v[8:9]
	s_waitcnt lgkmcnt(0)
	global_store_dwordx4 v[8:9], v[2:5], off offset:-256 sc1
.LBB1_62:
	s_andn2_saveexec_b64 s[6:7], s[6:7]
	s_cbranch_execz .LBB1_64
	v_add_u32_e32 v8, v6, v141
	v_lshl_or_b32 v8, v8, 7, v7
	s_waitcnt lgkmcnt(0)
	global_store_dwordx4 v8, v[2:5], s[12:13] sc1
.LBB1_64:
	s_or_b64 exec, exec, s[6:7]
	s_waitcnt lgkmcnt(0)
	v_add_u32_e32 v2, v137, v140
	v_add_u32_e32 v2, 0x4000, v2
	ds_read2_b64 v[2:5], v2 offset0:128 offset1:136
	s_and_saveexec_b64 s[6:7], s[4:5]
	s_xor_b64 s[6:7], exec, s[6:7]
	s_cbranch_execz .LBB1_66
	v_add_lshl_u32 v8, s3, v139, 8
	v_mov_b32_e32 v9, 0
	v_lshl_add_u64 v[8:9], v[130:131], 0, v[8:9]
	s_waitcnt lgkmcnt(0)
	global_store_dwordx4 v[8:9], v[2:5], off offset:-256 sc1
.LBB1_66:
	s_andn2_saveexec_b64 s[6:7], s[6:7]
	s_cbranch_execz .LBB1_68
	v_add_u32_e32 v8, v6, v139
	v_lshl_or_b32 v8, v8, 7, v7
	s_waitcnt lgkmcnt(0)
	global_store_dwordx4 v8, v[2:5], s[12:13] sc1
.LBB1_68:
	s_or_b64 exec, exec, s[6:7]
	s_waitcnt lgkmcnt(0)
	v_add_u32_e32 v2, v137, v138
	v_add_u32_e32 v2, 0x4000, v2
	ds_read2_b64 v[2:5], v2 offset0:128 offset1:136
	s_and_saveexec_b64 s[6:7], s[4:5]
	s_xor_b64 s[4:5], exec, s[6:7]
	s_cbranch_execz .LBB1_70
	v_add_lshl_u32 v6, s3, v136, 8
	v_mov_b32_e32 v7, 0
	v_lshl_add_u64 v[6:7], v[130:131], 0, v[6:7]
	s_waitcnt lgkmcnt(0)
	global_store_dwordx4 v[6:7], v[2:5], off offset:-256 sc1
.LBB1_70:
	s_andn2_saveexec_b64 s[4:5], s[4:5]
	s_cbranch_execz .LBB1_72
	v_add_u32_e32 v6, v6, v136
	v_lshl_or_b32 v6, v6, 7, v7
	s_waitcnt lgkmcnt(0)
	global_store_dwordx4 v6, v[2:5], s[12:13] sc1

_Z8k_gatherPK15HIP_vector_typeIiLj2EEPKjPKDv8_DF16_S7_PKfPf:
	s_lshr_b32 s3, s2, 3
	s_mulk_i32 s3, 0x1cf
	s_mul_hi_u32 s50, s3, 0xd1b71759
	s_lshr_b32 s50, s50, 10
	s_mulk_i32 s50, 0x4e2
	s_load_dwordx4 s[4:7], s[0:1], 0x0
	s_load_dwordx4 s[8:11], s[0:1], 0x10
	s_load_dwordx4 s[12:15], s[0:1], 0x20
	s_sub_i32 s3, s3, s50
	s_lshl_b32 s3, s3, 5
	s_and_b32 s51, s2, 7
	s_and_b32 s52, s2, 1
	s_lshr_b32 s53, s51, 1
	s_mul_i32 s53, s53, 0x9c40
	s_add_i32 s53, s53, s3
	v_and_b32_e32 v57, 7, v0
	v_lshrrev_b32_e32 v58, 3, v0
	v_lshlrev_b32_e32 v52, 4, v57
	v_add_u32_e32 v59, s3, v58
	v_add_u32_e32 v62, s53, v58
	v_lshlrev_b32_e32 v59, 3, v59
	v_lshl_add_u32 v63, v62, 8, v52
	v_lshl_add_u32 v54, v62, 9, v52
	s_mul_i32 s54, s51, 0x4e2000
	s_lshl_b32 s55, s52, 7
	s_lshl_b32 s56, s52, 8
	s_waitcnt lgkmcnt(0)
	global_load_dwordx2 v[60:61], v59, s[4:5]
	s_add_u32 s10, s10, s55
	s_addc_u32 s11, s11, 0
	global_load_dwordx4 v[8:11], v63, s[10:11] nt
	s_add_u32 s12, s12, s56
	s_addc_u32 s13, s13, 0
	global_load_dwordx4 v[4:7], v52, s[12:13]
	global_load_dwordx4 v[0:3], v52, s[12:13] offset:128
	s_add_u32 s14, s14, s56
	s_addc_u32 s15, s15, 0
	s_add_u32 s8, s8, s54
	s_addc_u32 s9, s9, 0
	s_mov_b32 s48, 0xffff
	v_mov_b32_e32 v56, 1.0
	s_waitcnt vmcnt(3)
	v_add_lshl_u32 v51, v60, v57, 2
	v_mov_b32_e32 v50, v61
	v_cmp_gt_i32_e32 vcc, v61, v57
	s_mov_b64 exec, vcc
	global_load_dword v49, v51, s[6:7]
	s_mov_b64 exec, -1
	s_waitcnt vmcnt(1)
	v_fma_mix_f32 v4, v8, v56, v4 op_sel_hi:[1,0,0]
	v_fma_mix_f32 v5, v8, v56, v5 op_sel:[1,0,0] op_sel_hi:[1,0,0]
	v_fma_mix_f32 v6, v9, v56, v6 op_sel_hi:[1,0,0]
	v_fma_mix_f32 v7, v9, v56, v7 op_sel:[1,0,0] op_sel_hi:[1,0,0]
	v_fma_mix_f32 v0, v10, v56, v0 op_sel_hi:[1,0,0]
	v_fma_mix_f32 v1, v10, v56, v1 op_sel:[1,0,0] op_sel_hi:[1,0,0]
	v_fma_mix_f32 v2, v11, v56, v2 op_sel_hi:[1,0,0]
	v_fma_mix_f32 v3, v11, v56, v3 op_sel:[1,0,0] op_sel_hi:[1,0,0]
	s_mov_b64 exec, -1
	s_waitcnt vmcnt(0)
	v_bfi_b32 v55, s48, v49, v48
	v_mov_b32_e32 v48, v49
	ds_swizzle_b32 v40, v55 offset:swizzle(BROADCAST,8,0)
	ds_swizzle_b32 v41, v55 offset:swizzle(BROADCAST,8,1)
	ds_swizzle_b32 v42, v55 offset:swizzle(BROADCAST,8,2)
	ds_swizzle_b32 v43, v55 offset:swizzle(BROADCAST,8,3)
	ds_swizzle_b32 v44, v55 offset:swizzle(BROADCAST,8,4)
	ds_swizzle_b32 v45, v55 offset:swizzle(BROADCAST,8,5)
	ds_swizzle_b32 v46, v55 offset:swizzle(BROADCAST,8,6)
	ds_swizzle_b32 v47, v55 offset:swizzle(BROADCAST,8,7)
	v_cmp_gt_i32_e64 s[32:33], v50, 0
	v_cmp_gt_i32_e64 s[34:35], v50, 1
	v_cmp_gt_i32_e64 s[36:37], v50, 2
	v_cmp_gt_i32_e64 s[38:39], v50, 3
	v_cmp_gt_i32_e64 s[40:41], v50, 4
	v_cmp_gt_i32_e64 s[42:43], v50, 5
	v_cmp_gt_i32_e64 s[44:45], v50, 6
	v_cmp_gt_i32_e64 s[46:47], v50, 7
	v_add_u32_e32 v50, -8, v50
	s_cmp_eq_u64 s[32:33], 0
	s_cbranch_scc1 .Lg_final
	v_cmp_gt_i32_e32 vcc, v50, v57
	v_add_u32_e32 v51, 32, v51
	s_mov_b64 exec, vcc
	global_load_dword v49, v51, s[6:7]
	s_waitcnt lgkmcnt(7)
	s_mov_b64 exec, s[32:33]
	v_and_b32_e32 v53, 0xffff, v40
	v_lshl_add_u32 v53, v53, 7, v52
	global_load_dwordx4 v[8:11], v53, s[8:9]
	s_waitcnt lgkmcnt(6)
	s_mov_b64 exec, s[34:35]
	v_and_b32_e32 v53, 0xffff, v41
	v_lshl_add_u32 v53, v53, 7, v52
	global_load_dwordx4 v[12:15], v53, s[8:9]
	s_waitcnt lgkmcnt(5)
	s_mov_b64 exec, s[36:37]
	v_and_b32_e32 v53, 0xffff, v42
	v_lshl_add_u32 v53, v53, 7, v52
	global_load_dwordx4 v[16:19], v53, s[8:9]
	s_waitcnt lgkmcnt(4)
	s_mov_b64 exec, s[38:39]
	v_and_b32_e32 v53, 0xffff, v43
	v_lshl_add_u32 v53, v53, 7, v52
	global_load_dwordx4 v[20:23], v53, s[8:9]
	s_waitcnt lgkmcnt(3)
	s_mov_b64 exec, s[40:41]
	v_and_b32_e32 v53, 0xffff, v44
	v_lshl_add_u32 v53, v53, 7, v52
	global_load_dwordx4 v[24:27], v53, s[8:9]
	s_waitcnt lgkmcnt(2)
	s_mov_b64 exec, s[42:43]
	v_and_b32_e32 v53, 0xffff, v45
	v_lshl_add_u32 v53, v53, 7, v52
	global_load_dwordx4 v[28:31], v53, s[8:9]
	s_waitcnt lgkmcnt(1)
	s_mov_b64 exec, s[44:45]
	v_and_b32_e32 v53, 0xffff, v46
	v_lshl_add_u32 v53, v53, 7, v52
	global_load_dwordx4 v[32:35], v53, s[8:9]
	s_waitcnt lgkmcnt(0)
	s_mov_b64 exec, s[46:47]
	v_and_b32_e32 v53, 0xffff, v47
	v_lshl_add_u32 v53, v53, 7, v52
	global_load_dwordx4 v[36:39], v53, s[8:9]
	s_mov_b64 s[16:17], s[32:33]
	s_mov_b64 s[18:19], s[34:35]
	s_mov_b64 s[20:21], s[36:37]
	s_mov_b64 s[22:23], s[38:39]
	s_mov_b64 s[24:25], s[40:41]
	s_mov_b64 s[26:27], s[42:43]
	s_mov_b64 s[28:29], s[44:45]
	s_mov_b64 s[30:31], s[46:47]
.Lg_top:
	s_mov_b64 exec, -1
	s_waitcnt vmcnt(8)
	v_bfi_b32 v55, s48, v49, v48
	v_mov_b32_e32 v48, v49
	ds_swizzle_b32 v40, v55 offset:swizzle(BROADCAST,8,0)
	ds_swizzle_b32 v41, v55 offset:swizzle(BROADCAST,8,1)
	ds_swizzle_b32 v42, v55 offset:swizzle(BROADCAST,8,2)
	ds_swizzle_b32 v43, v55 offset:swizzle(BROADCAST,8,3)
	ds_swizzle_b32 v44, v55 offset:swizzle(BROADCAST,8,4)
	ds_swizzle_b32 v45, v55 offset:swizzle(BROADCAST,8,5)
	ds_swizzle_b32 v46, v55 offset:swizzle(BROADCAST,8,6)
	ds_swizzle_b32 v47, v55 offset:swizzle(BROADCAST,8,7)
	v_cmp_gt_i32_e64 s[32:33], v50, 0
	v_cmp_gt_i32_e64 s[34:35], v50, 1
	v_cmp_gt_i32_e64 s[36:37], v50, 2
	v_cmp_gt_i32_e64 s[38:39], v50, 3
	v_cmp_gt_i32_e64 s[40:41], v50, 4
	v_cmp_gt_i32_e64 s[42:43], v50, 5
	v_cmp_gt_i32_e64 s[44:45], v50, 6
	v_cmp_gt_i32_e64 s[46:47], v50, 7
	v_add_u32_e32 v50, -8, v50
	s_cmp_eq_u64 s[32:33], 0
	s_cbranch_scc1 .Lg_drain
	v_cmp_gt_i32_e32 vcc, v50, v57
	v_add_u32_e32 v51, 32, v51
	s_mov_b64 exec, vcc
	global_load_dword v49, v51, s[6:7]
	s_waitcnt vmcnt(8) lgkmcnt(7)
	s_mov_b64 exec, s[16:17]
	v_fma_mix_f32 v4, v40, v8, v4 op_sel:[1,0,0] op_sel_hi:[1,1,0]
	v_fma_mix_f32 v5, v40, v8, v5 op_sel:[1,1,0] op_sel_hi:[1,1,0]
	v_fma_mix_f32 v6, v40, v9, v6 op_sel:[1,0,0] op_sel_hi:[1,1,0]
	v_fma_mix_f32 v7, v40, v9, v7 op_sel:[1,1,0] op_sel_hi:[1,1,0]
	v_fma_mix_f32 v0, v40, v10, v0 op_sel:[1,0,0] op_sel_hi:[1,1,0]
	v_fma_mix_f32 v1, v40, v10, v1 op_sel:[1,1,0] op_sel_hi:[1,1,0]
	v_fma_mix_f32 v2, v40, v11, v2 op_sel:[1,0,0] op_sel_hi:[1,1,0]
	v_fma_mix_f32 v3, v40, v11, v3 op_sel:[1,1,0] op_sel_hi:[1,1,0]
	s_mov_b64 exec, s[32:33]
	v_and_b32_e32 v53, 0xffff, v40
	v_lshl_add_u32 v53, v53, 7, v52
	global_load_dwordx4 v[8:11], v53, s[8:9]
	s_waitcnt vmcnt(8) lgkmcnt(6)
	s_mov_b64 exec, s[18:19]
	v_fma_mix_f32 v4, v41, v12, v4 op_sel:[1,0,0] op_sel_hi:[1,1,0]
	v_fma_mix_f32 v5, v41, v12, v5 op_sel:[1,1,0] op_sel_hi:[1,1,0]
	v_fma_mix_f32 v6, v41, v13, v6 op_sel:[1,0,0] op_sel_hi:[1,1,0]
	v_fma_mix_f32 v7, v41, v13, v7 op_sel:[1,1,0] op_sel_hi:[1,1,0]
	v_fma_mix_f32 v0, v41, v14, v0 op_sel:[1,0,0] op_sel_hi:[1,1,0]
	v_fma_mix_f32 v1, v41, v14, v1 op_sel:[1,1,0] op_sel_hi:[1,1,0]
	v_fma_mix_f32 v2, v41, v15, v2 op_sel:[1,0,0] op_sel_hi:[1,1,0]
	v_fma_mix_f32 v3, v41, v15, v3 op_sel:[1,1,0] op_sel_hi:[1,1,0]
	s_mov_b64 exec, s[34:35]
	v_and_b32_e32 v53, 0xffff, v41
	v_lshl_add_u32 v53, v53, 7, v52
	global_load_dwordx4 v[12:15], v53, s[8:9]
	s_waitcnt vmcnt(8) lgkmcnt(5)
	s_mov_b64 exec, s[20:21]
	v_fma_mix_f32 v4, v42, v16, v4 op_sel:[1,0,0] op_sel_hi:[1,1,0]
	v_fma_mix_f32 v5, v42, v16, v5 op_sel:[1,1,0] op_sel_hi:[1,1,0]
	v_fma_mix_f32 v6, v42, v17, v6 op_sel:[1,0,0] op_sel_hi:[1,1,0]
	v_fma_mix_f32 v7, v42, v17, v7 op_sel:[1,1,0] op_sel_hi:[1,1,0]
	v_fma_mix_f32 v0, v42, v18, v0 op_sel:[1,0,0] op_sel_hi:[1,1,0]
	v_fma_mix_f32 v1, v42, v18, v1 op_sel:[1,1,0] op_sel_hi:[1,1,0]
	v_fma_mix_f32 v2, v42, v19, v2 op_sel:[1,0,0] op_sel_hi:[1,1,0]
	v_fma_mix_f32 v3, v42, v19, v3 op_sel:[1,1,0] op_sel_hi:[1,1,0]
	s_mov_b64 exec, s[36:37]
	v_and_b32_e32 v53, 0xffff, v42
	v_lshl_add_u32 v53, v53, 7, v52
	global_load_dwordx4 v[16:19], v53, s[8:9]
	s_waitcnt vmcnt(8) lgkmcnt(4)
	s_mov_b64 exec, s[22:23]
	v_fma_mix_f32 v4, v43, v20, v4 op_sel:[1,0,0] op_sel_hi:[1,1,0]
	v_fma_mix_f32 v5, v43, v20, v5 op_sel:[1,1,0] op_sel_hi:[1,1,0]
	v_fma_mix_f32 v6, v43, v21, v6 op_sel:[1,0,0] op_sel_hi:[1,1,0]
	v_fma_mix_f32 v7, v43, v21, v7 op_sel:[1,1,0] op_sel_hi:[1,1,0]
	v_fma_mix_f32 v0, v43, v22, v0 op_sel:[1,0,0] op_sel_hi:[1,1,0]
	v_fma_mix_f32 v1, v43, v22, v1 op_sel:[1,1,0] op_sel_hi:[1,1,0]
	v_fma_mix_f32 v2, v43, v23, v2 op_sel:[1,0,0] op_sel_hi:[1,1,0]
	v_fma_mix_f32 v3, v43, v23, v3 op_sel:[1,1,0] op_sel_hi:[1,1,0]
	s_mov_b64 exec, s[38:39]
	v_and_b32_e32 v53, 0xffff, v43
	v_lshl_add_u32 v53, v53, 7, v52
	global_load_dwordx4 v[20:23], v53, s[8:9]
	s_waitcnt vmcnt(8) lgkmcnt(3)
	s_mov_b64 exec, s[24:25]
	v_fma_mix_f32 v4, v44, v24, v4 op_sel:[1,0,0] op_sel_hi:[1,1,0]
	v_fma_mix_f32 v5, v44, v24, v5 op_sel:[1,1,0] op_sel_hi:[1,1,0]
	v_fma_mix_f32 v6, v44, v25, v6 op_sel:[1,0,0] op_sel_hi:[1,1,0]
	v_fma_mix_f32 v7, v44, v25, v7 op_sel:[1,1,0] op_sel_hi:[1,1,0]
	v_fma_mix_f32 v0, v44, v26, v0 op_sel:[1,0,0] op_sel_hi:[1,1,0]
	v_fma_mix_f32 v1, v44, v26, v1 op_sel:[1,1,0] op_sel_hi:[1,1,0]
	v_fma_mix_f32 v2, v44, v27, v2 op_sel:[1,0,0] op_sel_hi:[1,1,0]
	v_fma_mix_f32 v3, v44, v27, v3 op_sel:[1,1,0] op_sel_hi:[1,1,0]
	s_mov_b64 exec, s[40:41]
	v_and_b32_e32 v53, 0xffff, v44
	v_lshl_add_u32 v53, v53, 7, v52
	global_load_dwordx4 v[24:27], v53, s[8:9]
	s_waitcnt vmcnt(8) lgkmcnt(2)
	s_mov_b64 exec, s[26:27]
	v_fma_mix_f32 v4, v45, v28, v4 op_sel:[1,0,0] op_sel_hi:[1,1,0]
	v_fma_mix_f32 v5, v45, v28, v5 op_sel:[1,1,0] op_sel_hi:[1,1,0]
	v_fma_mix_f32 v6, v45, v29, v6 op_sel:[1,0,0] op_sel_hi:[1,1,0]
	v_fma_mix_f32 v7, v45, v29, v7 op_sel:[1,1,0] op_sel_hi:[1,1,0]
	v_fma_mix_f32 v0, v45, v30, v0 op_sel:[1,0,0] op_sel_hi:[1,1,0]
	v_fma_mix_f32 v1, v45, v30, v1 op_sel:[1,1,0] op_sel_hi:[1,1,0]
	v_fma_mix_f32 v2, v45, v31, v2 op_sel:[1,0,0] op_sel_hi:[1,1,0]
	v_fma_mix_f32 v3, v45, v31, v3 op_sel:[1,1,0] op_sel_hi:[1,1,0]
	s_mov_b64 exec, s[42:43]
	v_and_b32_e32 v53, 0xffff, v45
	v_lshl_add_u32 v53, v53, 7, v52
	global_load_dwordx4 v[28:31], v53, s[8:9]
	s_waitcnt vmcnt(8) lgkmcnt(1)
	s_mov_b64 exec, s[28:29]
	v_fma_mix_f32 v4, v46, v32, v4 op_sel:[1,0,0] op_sel_hi:[1,1,0]
	v_fma_mix_f32 v5, v46, v32, v5 op_sel:[1,1,0] op_sel_hi:[1,1,0]
	v_fma_mix_f32 v6, v46, v33, v6 op_sel:[1,0,0] op_sel_hi:[1,1,0]
	v_fma_mix_f32 v7, v46, v33, v7 op_sel:[1,1,0] op_sel_hi:[1,1,0]
	v_fma_mix_f32 v0, v46, v34, v0 op_sel:[1,0,0] op_sel_hi:[1,1,0]
	v_fma_mix_f32 v1, v46, v34, v1 op_sel:[1,1,0] op_sel_hi:[1,1,0]
	v_fma_mix_f32 v2, v46, v35, v2 op_sel:[1,0,0] op_sel_hi:[1,1,0]
	v_fma_mix_f32 v3, v46, v35, v3 op_sel:[1,1,0] op_sel_hi:[1,1,0]
	s_mov_b64 exec, s[44:45]
	v_and_b32_e32 v53, 0xffff, v46
	v_lshl_add_u32 v53, v53, 7, v52
	global_load_dwordx4 v[32:35], v53, s[8:9]
	s_waitcnt vmcnt(8) lgkmcnt(0)
	s_mov_b64 exec, s[30:31]
	v_fma_mix_f32 v4, v47, v36, v4 op_sel:[1,0,0] op_sel_hi:[1,1,0]
	v_fma_mix_f32 v5, v47, v36, v5 op_sel:[1,1,0] op_sel_hi:[1,1,0]
	v_fma_mix_f32 v6, v47, v37, v6 op_sel:[1,0,0] op_sel_hi:[1,1,0]
	v_fma_mix_f32 v7, v47, v37, v7 op_sel:[1,1,0] op_sel_hi:[1,1,0]
	v_fma_mix_f32 v0, v47, v38, v0 op_sel:[1,0,0] op_sel_hi:[1,1,0]
	v_fma_mix_f32 v1, v47, v38, v1 op_sel:[1,1,0] op_sel_hi:[1,1,0]
	v_fma_mix_f32 v2, v47, v39, v2 op_sel:[1,0,0] op_sel_hi:[1,1,0]
	v_fma_mix_f32 v3, v47, v39, v3 op_sel:[1,1,0] op_sel_hi:[1,1,0]
	s_mov_b64 exec, s[46:47]
	v_and_b32_e32 v53, 0xffff, v47
	v_lshl_add_u32 v53, v53, 7, v52
	global_load_dwordx4 v[36:39], v53, s[8:9]
	s_mov_b64 s[16:17], s[32:33]
	s_mov_b64 s[18:19], s[34:35]
	s_mov_b64 s[20:21], s[36:37]
	s_mov_b64 s[22:23], s[38:39]
	s_mov_b64 s[24:25], s[40:41]
	s_mov_b64 s[26:27], s[42:43]
	s_mov_b64 s[28:29], s[44:45]
	s_mov_b64 s[30:31], s[46:47]
	s_branch .Lg_top
.Lg_drain:
	s_waitcnt vmcnt(7) lgkmcnt(7)
	s_mov_b64 exec, s[16:17]
	v_fma_mix_f32 v4, v40, v8, v4 op_sel:[1,0,0] op_sel_hi:[1,1,0]
	v_fma_mix_f32 v5, v40, v8, v5 op_sel:[1,1,0] op_sel_hi:[1,1,0]
	v_fma_mix_f32 v6, v40, v9, v6 op_sel:[1,0,0] op_sel_hi:[1,1,0]
	v_fma_mix_f32 v7, v40, v9, v7 op_sel:[1,1,0] op_sel_hi:[1,1,0]
	v_fma_mix_f32 v0, v40, v10, v0 op_sel:[1,0,0] op_sel_hi:[1,1,0]
	v_fma_mix_f32 v1, v40, v10, v1 op_sel:[1,1,0] op_sel_hi:[1,1,0]
	v_fma_mix_f32 v2, v40, v11, v2 op_sel:[1,0,0] op_sel_hi:[1,1,0]
	v_fma_mix_f32 v3, v40, v11, v3 op_sel:[1,1,0] op_sel_hi:[1,1,0]
	s_waitcnt vmcnt(6) lgkmcnt(6)
	s_mov_b64 exec, s[18:19]
	v_fma_mix_f32 v4, v41, v12, v4 op_sel:[1,0,0] op_sel_hi:[1,1,0]
	v_fma_mix_f32 v5, v41, v12, v5 op_sel:[1,1,0] op_sel_hi:[1,1,0]
	v_fma_mix_f32 v6, v41, v13, v6 op_sel:[1,0,0] op_sel_hi:[1,1,0]
	v_fma_mix_f32 v7, v41, v13, v7 op_sel:[1,1,0] op_sel_hi:[1,1,0]
	v_fma_mix_f32 v0, v41, v14, v0 op_sel:[1,0,0] op_sel_hi:[1,1,0]
	v_fma_mix_f32 v1, v41, v14, v1 op_sel:[1,1,0] op_sel_hi:[1,1,0]
	v_fma_mix_f32 v2, v41, v15, v2 op_sel:[1,0,0] op_sel_hi:[1,1,0]
	v_fma_mix_f32 v3, v41, v15, v3 op_sel:[1,1,0] op_sel_hi:[1,1,0]
	s_waitcnt vmcnt(5) lgkmcnt(5)
	s_mov_b64 exec, s[20:21]
	v_fma_mix_f32 v4, v42, v16, v4 op_sel:[1,0,0] op_sel_hi:[1,1,0]
	v_fma_mix_f32 v5, v42, v16, v5 op_sel:[1,1,0] op_sel_hi:[1,1,0]
	v_fma_mix_f32 v6, v42, v17, v6 op_sel:[1,0,0] op_sel_hi:[1,1,0]
	v_fma_mix_f32 v7, v42, v17, v7 op_sel:[1,1,0] op_sel_hi:[1,1,0]
	v_fma_mix_f32 v0, v42, v18, v0 op_sel:[1,0,0] op_sel_hi:[1,1,0]
	v_fma_mix_f32 v1, v42, v18, v1 op_sel:[1,1,0] op_sel_hi:[1,1,0]
	v_fma_mix_f32 v2, v42, v19, v2 op_sel:[1,0,0] op_sel_hi:[1,1,0]
	v_fma_mix_f32 v3, v42, v19, v3 op_sel:[1,1,0] op_sel_hi:[1,1,0]
	s_waitcnt vmcnt(4) lgkmcnt(4)
	s_mov_b64 exec, s[22:23]
	v_fma_mix_f32 v4, v43, v20, v4 op_sel:[1,0,0] op_sel_hi:[1,1,0]
	v_fma_mix_f32 v5, v43, v20, v5 op_sel:[1,1,0] op_sel_hi:[1,1,0]
	v_fma_mix_f32 v6, v43, v21, v6 op_sel:[1,0,0] op_sel_hi:[1,1,0]
	v_fma_mix_f32 v7, v43, v21, v7 op_sel:[1,1,0] op_sel_hi:[1,1,0]
	v_fma_mix_f32 v0, v43, v22, v0 op_sel:[1,0,0] op_sel_hi:[1,1,0]
	v_fma_mix_f32 v1, v43, v22, v1 op_sel:[1,1,0] op_sel_hi:[1,1,0]
	v_fma_mix_f32 v2, v43, v23, v2 op_sel:[1,0,0] op_sel_hi:[1,1,0]
	v_fma_mix_f32 v3, v43, v23, v3 op_sel:[1,1,0] op_sel_hi:[1,1,0]
	s_waitcnt vmcnt(3) lgkmcnt(3)
	s_mov_b64 exec, s[24:25]
	v_fma_mix_f32 v4, v44, v24, v4 op_sel:[1,0,0] op_sel_hi:[1,1,0]
	v_fma_mix_f32 v5, v44, v24, v5 op_sel:[1,1,0] op_sel_hi:[1,1,0]
	v_fma_mix_f32 v6, v44, v25, v6 op_sel:[1,0,0] op_sel_hi:[1,1,0]
	v_fma_mix_f32 v7, v44, v25, v7 op_sel:[1,1,0] op_sel_hi:[1,1,0]
	v_fma_mix_f32 v0, v44, v26, v0 op_sel:[1,0,0] op_sel_hi:[1,1,0]
	v_fma_mix_f32 v1, v44, v26, v1 op_sel:[1,1,0] op_sel_hi:[1,1,0]
	v_fma_mix_f32 v2, v44, v27, v2 op_sel:[1,0,0] op_sel_hi:[1,1,0]
	v_fma_mix_f32 v3, v44, v27, v3 op_sel:[1,1,0] op_sel_hi:[1,1,0]
	s_waitcnt vmcnt(2) lgkmcnt(2)
	s_mov_b64 exec, s[26:27]
	v_fma_mix_f32 v4, v45, v28, v4 op_sel:[1,0,0] op_sel_hi:[1,1,0]
	v_fma_mix_f32 v5, v45, v28, v5 op_sel:[1,1,0] op_sel_hi:[1,1,0]
	v_fma_mix_f32 v6, v45, v29, v6 op_sel:[1,0,0] op_sel_hi:[1,1,0]
	v_fma_mix_f32 v7, v45, v29, v7 op_sel:[1,1,0] op_sel_hi:[1,1,0]
	v_fma_mix_f32 v0, v45, v30, v0 op_sel:[1,0,0] op_sel_hi:[1,1,0]
	v_fma_mix_f32 v1, v45, v30, v1 op_sel:[1,1,0] op_sel_hi:[1,1,0]
	v_fma_mix_f32 v2, v45, v31, v2 op_sel:[1,0,0] op_sel_hi:[1,1,0]
	v_fma_mix_f32 v3, v45, v31, v3 op_sel:[1,1,0] op_sel_hi:[1,1,0]
	s_waitcnt vmcnt(1) lgkmcnt(1)
	s_mov_b64 exec, s[28:29]
	v_fma_mix_f32 v4, v46, v32, v4 op_sel:[1,0,0] op_sel_hi:[1,1,0]
	v_fma_mix_f32 v5, v46, v32, v5 op_sel:[1,1,0] op_sel_hi:[1,1,0]
	v_fma_mix_f32 v6, v46, v33, v6 op_sel:[1,0,0] op_sel_hi:[1,1,0]
	v_fma_mix_f32 v7, v46, v33, v7 op_sel:[1,1,0] op_sel_hi:[1,1,0]
	v_fma_mix_f32 v0, v46, v34, v0 op_sel:[1,0,0] op_sel_hi:[1,1,0]
	v_fma_mix_f32 v1, v46, v34, v1 op_sel:[1,1,0] op_sel_hi:[1,1,0]
	v_fma_mix_f32 v2, v46, v35, v2 op_sel:[1,0,0] op_sel_hi:[1,1,0]
	v_fma_mix_f32 v3, v46, v35, v3 op_sel:[1,1,0] op_sel_hi:[1,1,0]
	s_waitcnt vmcnt(0) lgkmcnt(0)
	s_mov_b64 exec, s[30:31]
	v_fma_mix_f32 v4, v47, v36, v4 op_sel:[1,0,0] op_sel_hi:[1,1,0]
	v_fma_mix_f32 v5, v47, v36, v5 op_sel:[1,1,0] op_sel_hi:[1,1,0]
	v_fma_mix_f32 v6, v47, v37, v6 op_sel:[1,0,0] op_sel_hi:[1,1,0]
	v_fma_mix_f32 v7, v47, v37, v7 op_sel:[1,1,0] op_sel_hi:[1,1,0]
	v_fma_mix_f32 v0, v47, v38, v0 op_sel:[1,0,0] op_sel_hi:[1,1,0]
	v_fma_mix_f32 v1, v47, v38, v1 op_sel:[1,1,0] op_sel_hi:[1,1,0]
	v_fma_mix_f32 v2, v47, v39, v2 op_sel:[1,0,0] op_sel_hi:[1,1,0]
	v_fma_mix_f32 v3, v47, v39, v3 op_sel:[1,1,0] op_sel_hi:[1,1,0]
.Lg_final:
	s_mov_b64 exec, -1
	global_store_dwordx4 v54, v[4:7], s[14:15] sc1
	global_store_dwordx4 v54, v[0:3], s[14:15] offset:128 sc1
	s_endpgm

	.amdhsa_kernel _Z8k_gatherPK15HIP_vector_typeIiLj2EEPKjPKDv8_DF16_S7_PKfPf
		.amdhsa_group_segment_fixed_size 0
		.amdhsa_private_segment_fixed_size 0
		.amdhsa_kernarg_size 48
		.amdhsa_user_sgpr_count 2
		.amdhsa_user_sgpr_dispatch_ptr 0
		.amdhsa_user_sgpr_queue_ptr 0
		.amdhsa_user_sgpr_kernarg_segment_ptr 1
		.amdhsa_user_sgpr_dispatch_id 0
		.amdhsa_user_sgpr_kernarg_preload_length 0
		.amdhsa_user_sgpr_kernarg_preload_offset 0
		.amdhsa_user_sgpr_private_segment_size 0
		.amdhsa_uses_dynamic_stack 0
		.amdhsa_enable_private_segment 0
		.amdhsa_system_sgpr_workgroup_id_x 1
		.amdhsa_system_sgpr_workgroup_id_y 0
		.amdhsa_system_sgpr_workgroup_id_z 0
		.amdhsa_system_sgpr_workgroup_info 0
		.amdhsa_system_vgpr_workitem_id 0
		.amdhsa_next_free_vgpr 64
		.amdhsa_next_free_sgpr 57
		.amdhsa_accum_offset 64
		.amdhsa_reserve_vcc 1
		.amdhsa_float_round_mode_32 0
		.amdhsa_float_round_mode_16_64 0
		.amdhsa_float_denorm_mode_32 3
		.amdhsa_float_denorm_mode_16_64 3
		.amdhsa_dx10_clamp 1
		.amdhsa_ieee_mode 1
		.amdhsa_fp16_overflow 0
		.amdhsa_tg_split 0
		.amdhsa_exception_fp_ieee_invalid_op 0
		.amdhsa_exception_fp_denorm_src 0
		.amdhsa_exception_fp_ieee_div_zero 0
		.amdhsa_exception_fp_ieee_overflow 0
		.amdhsa_exception_fp_ieee_underflow 0
		.amdhsa_exception_fp_ieee_inexact 0
		.amdhsa_exception_int_div_zero 0
	.end_amdhsa_kernel

amdhsa.kernels:
  - .agpr_count:     0
    .args:
      - .actual_access:  read_only
        .address_space:  global
        .offset:         0
        .size:           8
        .value_kind:     global_buffer
      - .actual_access:  read_only
        .address_space:  global
        .offset:         8
        .size:           8
        .value_kind:     global_buffer
      - .actual_access:  read_only
        .address_space:  global
        .offset:         16
        .size:           8
        .value_kind:     global_buffer
      - .actual_access:  write_only
        .address_space:  global
        .offset:         24
        .size:           8
        .value_kind:     global_buffer
      - .actual_access:  write_only
        .address_space:  global
        .offset:         32
        .size:           8
        .value_kind:     global_buffer
      - .actual_access:  read_only
        .address_space:  global
        .offset:         40
        .size:           8
        .value_kind:     global_buffer
      - .actual_access:  read_only
        .address_space:  global
        .offset:         48
        .size:           8
        .value_kind:     global_buffer
      - .actual_access:  write_only
        .address_space:  global
        .offset:         56
        .size:           8
        .value_kind:     global_buffer
      - .actual_access:  read_only
        .address_space:  global
        .offset:         64
        .size:           8
        .value_kind:     global_buffer
    .group_segment_fixed_size: 27200
    .kernarg_segment_align: 8
    .kernarg_segment_size: 72
    .language:       OpenCL C
    .language_version:
      - 2
      - 0
    .max_flat_workgroup_size: 1024
    .name:           _Z6k_partPKiS0_PKfP15HIP_vector_typeIiLj2EEPiS2_S2_PDv8_DF16_S6_
    .private_segment_fixed_size: 0
    .sgpr_count:     30
    .sgpr_spill_count: 0
    .symbol:         _Z6k_partPKiS0_PKfP15HIP_vector_typeIiLj2EEPiS2_S2_PDv8_DF16_S6_.kd
    .uniform_work_group_size: 1
    .uses_dynamic_stack: false
    .vgpr_count:     30
    .vgpr_spill_count: 0
    .wavefront_size: 64
  - .agpr_count:     0
    .args:
      - .actual_access:  read_only
        .address_space:  global
        .offset:         0
        .size:           8
        .value_kind:     global_buffer
      - .actual_access:  read_only
        .address_space:  global
        .offset:         8
        .size:           8
        .value_kind:     global_buffer
      - .actual_access:  write_only
        .address_space:  global
        .offset:         16
        .size:           8
        .value_kind:     global_buffer
      - .actual_access:  write_only
        .address_space:  global
        .offset:         24
        .size:           8
        .value_kind:     global_buffer
      - .actual_access:  read_only
        .address_space:  global
        .offset:         32
        .size:           8
        .value_kind:     global_buffer
      - .actual_access:  read_only
        .address_space:  global
        .offset:         40
        .size:           8
        .value_kind:     global_buffer
      - .actual_access:  read_only
        .address_space:  global
        .offset:         48
        .size:           8
        .value_kind:     global_buffer
      - .actual_access:  write_only
        .address_space:  global
        .offset:         56
        .size:           8
        .value_kind:     global_buffer
      - .actual_access:  write_only
        .address_space:  global
        .offset:         64
        .size:           8
        .value_kind:     global_buffer
    .group_segment_fixed_size: 51200
    .kernarg_segment_align: 8
    .kernarg_segment_size: 72
    .language:       OpenCL C
    .language_version:
      - 2
      - 0
    .max_flat_workgroup_size: 256
    .name:           _Z6k_gemmPKfPKDv8_DF16_PDF16_S4_PK15HIP_vector_typeIiLj2EEPKiPiPS6_Pj
    .private_segment_fixed_size: 0
    .sgpr_count:     44
    .sgpr_spill_count: 0
    .symbol:         _Z6k_gemmPKfPKDv8_DF16_PDF16_S4_PK15HIP_vector_typeIiLj2EEPKiPiPS6_Pj.kd
    .uniform_work_group_size: 1
    .uses_dynamic_stack: false
    .vgpr_count:     166
    .vgpr_spill_count: 0
    .wavefront_size: 64
  - .agpr_count:     0
    .args:
      - .actual_access:  read_only
        .address_space:  global
        .offset:         0
        .size:           8
        .value_kind:     global_buffer
      - .actual_access:  read_only
        .address_space:  global
        .offset:         8
        .size:           8
        .value_kind:     global_buffer
      - .actual_access:  read_only
        .address_space:  global
        .offset:         16
        .size:           8
        .value_kind:     global_buffer
      - .actual_access:  read_only
        .address_space:  global
        .offset:         24
        .size:           8
        .value_kind:     global_buffer
      - .actual_access:  read_only
        .address_space:  global
        .offset:         32
        .size:           8
        .value_kind:     global_buffer
      - .actual_access:  write_only
        .address_space:  global
        .offset:         40
        .size:           8
        .value_kind:     global_buffer
    .group_segment_fixed_size: 0
    .kernarg_segment_align: 8
    .kernarg_segment_size: 48
    .language:       OpenCL C
    .language_version:
      - 2
      - 0
    .max_flat_workgroup_size: 256
    .name:           _Z8k_gatherPK15HIP_vector_typeIiLj2EEPKjPKDv8_DF16_S7_PKfPf
    .private_segment_fixed_size: 0
    .sgpr_count:     63
    .sgpr_spill_count: 0
    .symbol:         _Z8k_gatherPK15HIP_vector_typeIiLj2EEPKjPKDv8_DF16_S7_PKfPf.kd
    .uniform_work_group_size: 1
    .uses_dynamic_stack: false
    .vgpr_count:     64
    .vgpr_spill_count: 0
    .wavefront_size: 64
